# phase-6 epilogue hand-pipelined: x quads requested 8 steps ahead, counted waits (on top of the MoE A-pairing version)
# speedup vs baseline: 1.0040x; 1.0040x over previous
.LBB0_610:
	s_lshr_b32 s2, s56, 4
	v_mbcnt_lo_u32_b32 v1, -1, 0
	v_mbcnt_hi_u32_b32 v1, -1, v1
	s_or_b32 s33, s57, s37
	v_ashrrev_i32_e32 v130, 2, v1
	s_mul_i32 s2, s2, 0xc000
	v_and_b32_e32 v130, -4, v130
	s_add_u32 s2, s28, s2
	v_add_u32_e32 v132, s33, v130
	s_addc_u32 s33, s29, 0
	s_add_u32 s38, s2, 0x204000
	s_addc_u32 s39, s33, 0
	s_add_i32 s55, s55, s3
	v_and_or_b32 v178, v1, 15, s55
	v_ashrrev_i32_e32 v133, 31, v132
	v_lshlrev_b64 v[130:131], 11, v[178:179]
	v_lshl_add_u64 v[134:135], v[132:133], 2, s[38:39]
	v_lshlrev_b32_e32 v134, 2, v132
	v_lshl_add_u32 v135, v130, 2, v134
	v_mov_b32_e32 v136, v135
	v_mov_b32_e32 v137, v135
	global_load_dwordx4 v[138:141], v134, s[38:39]
	global_load_dwordx4 v[146:149], v136, s[52:53]
	v_add_u32_e32 v136, 0x20000, v136
	global_load_dwordx4 v[150:153], v136, s[52:53]
	v_add_u32_e32 v136, 0x20000, v136
	global_load_dwordx4 v[154:157], v136, s[52:53]
	v_add_u32_e32 v136, 0x20000, v136
	global_load_dwordx4 v[158:161], v136, s[52:53]
	v_add_u32_e32 v136, 0x20000, v136
	global_load_dwordx4 v[162:165], v136, s[52:53]
	v_add_u32_e32 v136, 0x20000, v136
	global_load_dwordx4 v[166:169], v136, s[52:53]
	v_add_u32_e32 v136, 0x20000, v136
	global_load_dwordx4 v[170:173], v136, s[52:53]
	v_add_u32_e32 v136, 0x20000, v136
	global_load_dwordx4 v[174:177], v136, s[52:53]
	v_add_u32_e32 v136, 0x20000, v136
	v_mov_b32_e32 v136, v135
	global_load_dwordx4 v[142:145], v134, s[38:39] offset:64
	s_waitcnt vmcnt(9)
	v_pk_add_f32 v[138:139], v[138:139], 1.0 op_sel_hi:[1,0]
	v_pk_add_f32 v[140:141], v[140:141], 1.0 op_sel_hi:[1,0]
	s_waitcnt vmcnt(8)
	v_pk_mul_f32 v[126:127], v[126:127], v[138:139]
	v_pk_mul_f32 v[128:129], v[128:129], v[140:141]
	v_pk_fma_f32 v[126:127], v[146:147], s[36:37], v[126:127] op_sel_hi:[1,0,1]
	v_pk_fma_f32 v[128:129], v[148:149], s[36:37], v[128:129] op_sel_hi:[1,0,1]
	global_store_dwordx4 v137, v[126:129], s[10:11]
	global_load_dwordx4 v[146:149], v136, s[52:53] offset:64
	v_add_u32_e32 v136, 0x20000, v136
	v_add_u32_e32 v137, 0x20000, v137
	s_waitcnt vmcnt(9)
	v_pk_mul_f32 v[122:123], v[122:123], v[138:139]
	v_pk_mul_f32 v[124:125], v[124:125], v[140:141]
	v_pk_fma_f32 v[122:123], v[150:151], s[36:37], v[122:123] op_sel_hi:[1,0,1]
	v_pk_fma_f32 v[124:125], v[152:153], s[36:37], v[124:125] op_sel_hi:[1,0,1]
	global_store_dwordx4 v137, v[122:125], s[10:11]
	global_load_dwordx4 v[150:153], v136, s[52:53] offset:64
	v_add_u32_e32 v136, 0x20000, v136
	v_add_u32_e32 v137, 0x20000, v137
	s_waitcnt vmcnt(10)
	v_pk_mul_f32 v[118:119], v[118:119], v[138:139]
	v_pk_mul_f32 v[120:121], v[120:121], v[140:141]
	v_pk_fma_f32 v[118:119], v[154:155], s[36:37], v[118:119] op_sel_hi:[1,0,1]
	v_pk_fma_f32 v[120:121], v[156:157], s[36:37], v[120:121] op_sel_hi:[1,0,1]
	global_store_dwordx4 v137, v[118:121], s[10:11]
	global_load_dwordx4 v[154:157], v136, s[52:53] offset:64
	v_add_u32_e32 v136, 0x20000, v136
	v_add_u32_e32 v137, 0x20000, v137
	s_waitcnt vmcnt(11)
	v_pk_mul_f32 v[114:115], v[114:115], v[138:139]
	v_pk_mul_f32 v[116:117], v[116:117], v[140:141]
	v_pk_fma_f32 v[114:115], v[158:159], s[36:37], v[114:115] op_sel_hi:[1,0,1]
	v_pk_fma_f32 v[116:117], v[160:161], s[36:37], v[116:117] op_sel_hi:[1,0,1]
	global_store_dwordx4 v137, v[114:117], s[10:11]
	global_load_dwordx4 v[158:161], v136, s[52:53] offset:64
	v_add_u32_e32 v136, 0x20000, v136
	v_add_u32_e32 v137, 0x20000, v137
	s_waitcnt vmcnt(12)
	v_pk_mul_f32 v[110:111], v[110:111], v[138:139]
	v_pk_mul_f32 v[112:113], v[112:113], v[140:141]
	v_pk_fma_f32 v[110:111], v[162:163], s[36:37], v[110:111] op_sel_hi:[1,0,1]
	v_pk_fma_f32 v[112:113], v[164:165], s[36:37], v[112:113] op_sel_hi:[1,0,1]
	global_store_dwordx4 v137, v[110:113], s[10:11]
	global_load_dwordx4 v[162:165], v136, s[52:53] offset:64
	v_add_u32_e32 v136, 0x20000, v136
	v_add_u32_e32 v137, 0x20000, v137
	s_waitcnt vmcnt(13)
	v_pk_mul_f32 v[106:107], v[106:107], v[138:139]
	v_pk_mul_f32 v[108:109], v[108:109], v[140:141]
	v_pk_fma_f32 v[106:107], v[166:167], s[36:37], v[106:107] op_sel_hi:[1,0,1]
	v_pk_fma_f32 v[108:109], v[168:169], s[36:37], v[108:109] op_sel_hi:[1,0,1]
	global_store_dwordx4 v137, v[106:109], s[10:11]
	global_load_dwordx4 v[166:169], v136, s[52:53] offset:64
	v_add_u32_e32 v136, 0x20000, v136
	v_add_u32_e32 v137, 0x20000, v137
	s_waitcnt vmcnt(14)
	v_pk_mul_f32 v[98:99], v[98:99], v[138:139]
	v_pk_mul_f32 v[100:101], v[100:101], v[140:141]
	v_pk_fma_f32 v[98:99], v[170:171], s[36:37], v[98:99] op_sel_hi:[1,0,1]
	v_pk_fma_f32 v[100:101], v[172:173], s[36:37], v[100:101] op_sel_hi:[1,0,1]
	global_store_dwordx4 v137, v[98:101], s[10:11]
	global_load_dwordx4 v[170:173], v136, s[52:53] offset:64
	v_add_u32_e32 v136, 0x20000, v136
	v_add_u32_e32 v137, 0x20000, v137
	s_waitcnt vmcnt(15)
	v_pk_mul_f32 v[90:91], v[90:91], v[138:139]
	v_pk_mul_f32 v[92:93], v[92:93], v[140:141]
	v_pk_fma_f32 v[90:91], v[174:175], s[36:37], v[90:91] op_sel_hi:[1,0,1]
	v_pk_fma_f32 v[92:93], v[176:177], s[36:37], v[92:93] op_sel_hi:[1,0,1]
	global_store_dwordx4 v137, v[90:93], s[10:11]
	global_load_dwordx4 v[174:177], v136, s[52:53] offset:64
	v_add_u32_e32 v136, 0x20000, v136
	v_add_u32_e32 v137, 0x20000, v137
	v_mov_b32_e32 v136, v135
	v_mov_b32_e32 v137, v135
	global_load_dwordx4 v[138:141], v134, s[38:39] offset:128
	s_waitcnt vmcnt(17)
	v_pk_add_f32 v[142:143], v[142:143], 1.0 op_sel_hi:[1,0]
	v_pk_add_f32 v[144:145], v[144:145], 1.0 op_sel_hi:[1,0]
	s_waitcnt vmcnt(15)
	v_pk_mul_f32 v[102:103], v[102:103], v[142:143]
	v_pk_mul_f32 v[104:105], v[104:105], v[144:145]
	v_pk_fma_f32 v[102:103], v[146:147], s[36:37], v[102:103] op_sel_hi:[1,0,1]
	v_pk_fma_f32 v[104:105], v[148:149], s[36:37], v[104:105] op_sel_hi:[1,0,1]
	global_store_dwordx4 v137, v[102:105], s[10:11] offset:64
	global_load_dwordx4 v[146:149], v136, s[52:53] offset:128
	v_add_u32_e32 v136, 0x20000, v136
	v_add_u32_e32 v137, 0x20000, v137
	s_waitcnt vmcnt(15)
	v_pk_mul_f32 v[94:95], v[94:95], v[142:143]
	v_pk_mul_f32 v[96:97], v[96:97], v[144:145]
	v_pk_fma_f32 v[94:95], v[150:151], s[36:37], v[94:95] op_sel_hi:[1,0,1]
	v_pk_fma_f32 v[96:97], v[152:153], s[36:37], v[96:97] op_sel_hi:[1,0,1]
	global_store_dwordx4 v137, v[94:97], s[10:11] offset:64
	global_load_dwordx4 v[150:153], v136, s[52:53] offset:128
	v_add_u32_e32 v136, 0x20000, v136
	v_add_u32_e32 v137, 0x20000, v137
	s_waitcnt vmcnt(15)
	v_pk_mul_f32 v[86:87], v[86:87], v[142:143]
	v_pk_mul_f32 v[88:89], v[88:89], v[144:145]
	v_pk_fma_f32 v[86:87], v[154:155], s[36:37], v[86:87] op_sel_hi:[1,0,1]
	v_pk_fma_f32 v[88:89], v[156:157], s[36:37], v[88:89] op_sel_hi:[1,0,1]
	global_store_dwordx4 v137, v[86:89], s[10:11] offset:64
	global_load_dwordx4 v[154:157], v136, s[52:53] offset:128
	v_add_u32_e32 v136, 0x20000, v136
	v_add_u32_e32 v137, 0x20000, v137
	s_waitcnt vmcnt(15)
	v_pk_mul_f32 v[82:83], v[82:83], v[142:143]
	v_pk_mul_f32 v[84:85], v[84:85], v[144:145]
	v_pk_fma_f32 v[82:83], v[158:159], s[36:37], v[82:83] op_sel_hi:[1,0,1]
	v_pk_fma_f32 v[84:85], v[160:161], s[36:37], v[84:85] op_sel_hi:[1,0,1]
	global_store_dwordx4 v137, v[82:85], s[10:11] offset:64
	global_load_dwordx4 v[158:161], v136, s[52:53] offset:128
	v_add_u32_e32 v136, 0x20000, v136
	v_add_u32_e32 v137, 0x20000, v137
	s_waitcnt vmcnt(15)
	v_pk_mul_f32 v[78:79], v[78:79], v[142:143]
	v_pk_mul_f32 v[80:81], v[80:81], v[144:145]
	v_pk_fma_f32 v[78:79], v[162:163], s[36:37], v[78:79] op_sel_hi:[1,0,1]
	v_pk_fma_f32 v[80:81], v[164:165], s[36:37], v[80:81] op_sel_hi:[1,0,1]
	global_store_dwordx4 v137, v[78:81], s[10:11] offset:64
	global_load_dwordx4 v[162:165], v136, s[52:53] offset:128
	v_add_u32_e32 v136, 0x20000, v136
	v_add_u32_e32 v137, 0x20000, v137
	s_waitcnt vmcnt(15)
	v_pk_mul_f32 v[74:75], v[74:75], v[142:143]
	v_pk_mul_f32 v[76:77], v[76:77], v[144:145]
	v_pk_fma_f32 v[74:75], v[166:167], s[36:37], v[74:75] op_sel_hi:[1,0,1]
	v_pk_fma_f32 v[76:77], v[168:169], s[36:37], v[76:77] op_sel_hi:[1,0,1]
	global_store_dwordx4 v137, v[74:77], s[10:11] offset:64
	global_load_dwordx4 v[166:169], v136, s[52:53] offset:128
	v_add_u32_e32 v136, 0x20000, v136
	v_add_u32_e32 v137, 0x20000, v137
	s_waitcnt vmcnt(15)
	v_pk_mul_f32 v[66:67], v[66:67], v[142:143]
	v_pk_mul_f32 v[68:69], v[68:69], v[144:145]
	v_pk_fma_f32 v[66:67], v[170:171], s[36:37], v[66:67] op_sel_hi:[1,0,1]
	v_pk_fma_f32 v[68:69], v[172:173], s[36:37], v[68:69] op_sel_hi:[1,0,1]
	global_store_dwordx4 v137, v[66:69], s[10:11] offset:64
	global_load_dwordx4 v[170:173], v136, s[52:53] offset:128
	v_add_u32_e32 v136, 0x20000, v136
	v_add_u32_e32 v137, 0x20000, v137
	s_waitcnt vmcnt(15)
	v_pk_mul_f32 v[58:59], v[58:59], v[142:143]
	v_pk_mul_f32 v[60:61], v[60:61], v[144:145]
	v_pk_fma_f32 v[58:59], v[174:175], s[36:37], v[58:59] op_sel_hi:[1,0,1]
	v_pk_fma_f32 v[60:61], v[176:177], s[36:37], v[60:61] op_sel_hi:[1,0,1]
	global_store_dwordx4 v137, v[58:61], s[10:11] offset:64
	global_load_dwordx4 v[174:177], v136, s[52:53] offset:128
	v_add_u32_e32 v136, 0x20000, v136
	v_add_u32_e32 v137, 0x20000, v137
	v_mov_b32_e32 v136, v135
	v_mov_b32_e32 v137, v135
	global_load_dwordx4 v[142:145], v134, s[38:39] offset:192
	s_waitcnt vmcnt(17)
	v_pk_add_f32 v[138:139], v[138:139], 1.0 op_sel_hi:[1,0]
	v_pk_add_f32 v[140:141], v[140:141], 1.0 op_sel_hi:[1,0]
	s_waitcnt vmcnt(15)
	v_pk_mul_f32 v[70:71], v[70:71], v[138:139]
	v_pk_mul_f32 v[72:73], v[72:73], v[140:141]
	v_pk_fma_f32 v[70:71], v[146:147], s[36:37], v[70:71] op_sel_hi:[1,0,1]
	v_pk_fma_f32 v[72:73], v[148:149], s[36:37], v[72:73] op_sel_hi:[1,0,1]
	global_store_dwordx4 v137, v[70:73], s[10:11] offset:128
	global_load_dwordx4 v[146:149], v136, s[52:53] offset:192
	v_add_u32_e32 v136, 0x20000, v136
	v_add_u32_e32 v137, 0x20000, v137
	s_waitcnt vmcnt(15)
	v_pk_mul_f32 v[62:63], v[62:63], v[138:139]
	v_pk_mul_f32 v[64:65], v[64:65], v[140:141]
	v_pk_fma_f32 v[62:63], v[150:151], s[36:37], v[62:63] op_sel_hi:[1,0,1]
	v_pk_fma_f32 v[64:65], v[152:153], s[36:37], v[64:65] op_sel_hi:[1,0,1]
	global_store_dwordx4 v137, v[62:65], s[10:11] offset:128
	global_load_dwordx4 v[150:153], v136, s[52:53] offset:192
	v_add_u32_e32 v136, 0x20000, v136
	v_add_u32_e32 v137, 0x20000, v137
	s_waitcnt vmcnt(15)
	v_pk_mul_f32 v[54:55], v[54:55], v[138:139]
	v_pk_mul_f32 v[56:57], v[56:57], v[140:141]
	v_pk_fma_f32 v[54:55], v[154:155], s[36:37], v[54:55] op_sel_hi:[1,0,1]
	v_pk_fma_f32 v[56:57], v[156:157], s[36:37], v[56:57] op_sel_hi:[1,0,1]
	global_store_dwordx4 v137, v[54:57], s[10:11] offset:128
	global_load_dwordx4 v[154:157], v136, s[52:53] offset:192
	v_add_u32_e32 v136, 0x20000, v136
	v_add_u32_e32 v137, 0x20000, v137
	s_waitcnt vmcnt(15)
	v_pk_mul_f32 v[50:51], v[50:51], v[138:139]
	v_pk_mul_f32 v[52:53], v[52:53], v[140:141]
	v_pk_fma_f32 v[50:51], v[158:159], s[36:37], v[50:51] op_sel_hi:[1,0,1]
	v_pk_fma_f32 v[52:53], v[160:161], s[36:37], v[52:53] op_sel_hi:[1,0,1]
	global_store_dwordx4 v137, v[50:53], s[10:11] offset:128
	global_load_dwordx4 v[158:161], v136, s[52:53] offset:192
	v_add_u32_e32 v136, 0x20000, v136
	v_add_u32_e32 v137, 0x20000, v137
	s_waitcnt vmcnt(15)
	v_pk_mul_f32 v[46:47], v[46:47], v[138:139]
	v_pk_mul_f32 v[48:49], v[48:49], v[140:141]
	v_pk_fma_f32 v[46:47], v[162:163], s[36:37], v[46:47] op_sel_hi:[1,0,1]
	v_pk_fma_f32 v[48:49], v[164:165], s[36:37], v[48:49] op_sel_hi:[1,0,1]
	global_store_dwordx4 v137, v[46:49], s[10:11] offset:128
	global_load_dwordx4 v[162:165], v136, s[52:53] offset:192
	v_add_u32_e32 v136, 0x20000, v136
	v_add_u32_e32 v137, 0x20000, v137
	s_waitcnt vmcnt(15)
	v_pk_mul_f32 v[42:43], v[42:43], v[138:139]
	v_pk_mul_f32 v[44:45], v[44:45], v[140:141]
	v_pk_fma_f32 v[42:43], v[166:167], s[36:37], v[42:43] op_sel_hi:[1,0,1]
	v_pk_fma_f32 v[44:45], v[168:169], s[36:37], v[44:45] op_sel_hi:[1,0,1]
	global_store_dwordx4 v137, v[42:45], s[10:11] offset:128
	global_load_dwordx4 v[166:169], v136, s[52:53] offset:192
	v_add_u32_e32 v136, 0x20000, v136
	v_add_u32_e32 v137, 0x20000, v137
	s_waitcnt vmcnt(15)
	v_pk_mul_f32 v[34:35], v[34:35], v[138:139]
	v_pk_mul_f32 v[36:37], v[36:37], v[140:141]
	v_pk_fma_f32 v[34:35], v[170:171], s[36:37], v[34:35] op_sel_hi:[1,0,1]
	v_pk_fma_f32 v[36:37], v[172:173], s[36:37], v[36:37] op_sel_hi:[1,0,1]
	global_store_dwordx4 v137, v[34:37], s[10:11] offset:128
	global_load_dwordx4 v[170:173], v136, s[52:53] offset:192
	v_add_u32_e32 v136, 0x20000, v136
	v_add_u32_e32 v137, 0x20000, v137
	s_waitcnt vmcnt(15)
	v_pk_mul_f32 v[26:27], v[26:27], v[138:139]
	v_pk_mul_f32 v[28:29], v[28:29], v[140:141]
	v_pk_fma_f32 v[26:27], v[174:175], s[36:37], v[26:27] op_sel_hi:[1,0,1]
	v_pk_fma_f32 v[28:29], v[176:177], s[36:37], v[28:29] op_sel_hi:[1,0,1]
	global_store_dwordx4 v137, v[26:29], s[10:11] offset:128
	global_load_dwordx4 v[174:177], v136, s[52:53] offset:192
	v_add_u32_e32 v136, 0x20000, v136
	v_add_u32_e32 v137, 0x20000, v137
	v_mov_b32_e32 v136, v135
	v_mov_b32_e32 v137, v135
	s_waitcnt vmcnt(16)
	v_pk_add_f32 v[142:143], v[142:143], 1.0 op_sel_hi:[1,0]
	v_pk_add_f32 v[144:145], v[144:145], 1.0 op_sel_hi:[1,0]
	s_waitcnt vmcnt(14)
	v_pk_mul_f32 v[38:39], v[38:39], v[142:143]
	v_pk_mul_f32 v[40:41], v[40:41], v[144:145]
	v_pk_fma_f32 v[38:39], v[146:147], s[36:37], v[38:39] op_sel_hi:[1,0,1]
	v_pk_fma_f32 v[40:41], v[148:149], s[36:37], v[40:41] op_sel_hi:[1,0,1]
	global_store_dwordx4 v137, v[38:41], s[10:11] offset:192
	v_add_u32_e32 v137, 0x20000, v137
	s_waitcnt vmcnt(13)
	v_pk_mul_f32 v[30:31], v[30:31], v[142:143]
	v_pk_mul_f32 v[32:33], v[32:33], v[144:145]
	v_pk_fma_f32 v[30:31], v[150:151], s[36:37], v[30:31] op_sel_hi:[1,0,1]
	v_pk_fma_f32 v[32:33], v[152:153], s[36:37], v[32:33] op_sel_hi:[1,0,1]
	global_store_dwordx4 v137, v[30:33], s[10:11] offset:192
	v_add_u32_e32 v137, 0x20000, v137
	s_waitcnt vmcnt(12)
	v_pk_mul_f32 v[22:23], v[22:23], v[142:143]
	v_pk_mul_f32 v[24:25], v[24:25], v[144:145]
	v_pk_fma_f32 v[22:23], v[154:155], s[36:37], v[22:23] op_sel_hi:[1,0,1]
	v_pk_fma_f32 v[24:25], v[156:157], s[36:37], v[24:25] op_sel_hi:[1,0,1]
	global_store_dwordx4 v137, v[22:25], s[10:11] offset:192
	v_add_u32_e32 v137, 0x20000, v137
	s_waitcnt vmcnt(11)
	v_pk_mul_f32 v[18:19], v[18:19], v[142:143]
	v_pk_mul_f32 v[20:21], v[20:21], v[144:145]
	v_pk_fma_f32 v[18:19], v[158:159], s[36:37], v[18:19] op_sel_hi:[1,0,1]
	v_pk_fma_f32 v[20:21], v[160:161], s[36:37], v[20:21] op_sel_hi:[1,0,1]
	global_store_dwordx4 v137, v[18:21], s[10:11] offset:192
	v_add_u32_e32 v137, 0x20000, v137
	s_waitcnt vmcnt(10)
	v_pk_mul_f32 v[14:15], v[14:15], v[142:143]
	v_pk_mul_f32 v[16:17], v[16:17], v[144:145]
	v_pk_fma_f32 v[14:15], v[162:163], s[36:37], v[14:15] op_sel_hi:[1,0,1]
	v_pk_fma_f32 v[16:17], v[164:165], s[36:37], v[16:17] op_sel_hi:[1,0,1]
	global_store_dwordx4 v137, v[14:17], s[10:11] offset:192
	v_add_u32_e32 v137, 0x20000, v137
	s_waitcnt vmcnt(9)
	v_pk_mul_f32 v[10:11], v[10:11], v[142:143]
	v_pk_mul_f32 v[12:13], v[12:13], v[144:145]
	v_pk_fma_f32 v[10:11], v[166:167], s[36:37], v[10:11] op_sel_hi:[1,0,1]
	v_pk_fma_f32 v[12:13], v[168:169], s[36:37], v[12:13] op_sel_hi:[1,0,1]
	global_store_dwordx4 v137, v[10:13], s[10:11] offset:192
	v_add_u32_e32 v137, 0x20000, v137
	s_waitcnt vmcnt(8)
	v_pk_mul_f32 v[6:7], v[6:7], v[142:143]
	v_pk_mul_f32 v[8:9], v[8:9], v[144:145]
	v_pk_fma_f32 v[6:7], v[170:171], s[36:37], v[6:7] op_sel_hi:[1,0,1]
	v_pk_fma_f32 v[8:9], v[172:173], s[36:37], v[8:9] op_sel_hi:[1,0,1]
	global_store_dwordx4 v137, v[6:9], s[10:11] offset:192
	v_add_u32_e32 v137, 0x20000, v137
	s_waitcnt vmcnt(7)
	v_pk_mul_f32 v[2:3], v[2:3], v[142:143]
	v_pk_mul_f32 v[4:5], v[4:5], v[144:145]
	v_pk_fma_f32 v[2:3], v[174:175], s[36:37], v[2:3] op_sel_hi:[1,0,1]
	v_pk_fma_f32 v[4:5], v[176:177], s[36:37], v[4:5] op_sel_hi:[1,0,1]
	global_store_dwordx4 v137, v[2:5], s[10:11] offset:192
	v_add_u32_e32 v137, 0x20000, v137
	v_mov_b32_e32 v136, v135
	v_mov_b32_e32 v137, v135
	s_add_i32 s1, s1, s0
	s_cmpk_lt_i32 s1, 0x100
	s_cbranch_scc0 .LBB0_623
